# ret-scan: 2-deep global prefetch (second register set, fast path when no further unit) + pipelined LDS fragment reads
# baseline (speedup 1.0000x reference)
; #define LAS __attribute__((address_space(3)))
; __device__ __forceinline__ void phase_ret_scan(const bf16* PROJ, bf16* O, LAS unsigned char* lds, int tid, int vcu, int G) {
;     ...
;     for (int unit = vcu; unit < NB * RT_H * 8; unit += G) {
;         const int b = unit >> 6, h = (unit >> 3) & 7, vsl = unit & 7;
;         const float lg = __log2f(1.0f - exp2f(-5.0f - (float)h));
;         const float g64 = exp2f(64.0f * lg);
;         f32x16 S[2][2];
; #pragma unroll
;         for (int a = 0; a < 2; ++a)
; #pragma unroll
;             for (int c = 0; c < 2; ++c) S[a][c] = zero16();
;         for (int i = tid; i < 33792 / 16; i += 512) *(LAS v4u*)(lds + ST + i * 16) = (v4u){0u, 0u, 0u, 0u};
.LBB0_569:
	s_add_i32 s4, s79, s85
	s_cmpk_lt_i32 s4, 0x100
	s_cbranch_scc0 .Lrf_569
	s_and_saveexec_b64 s[4:5], s[40:41]
	s_cbranch_execz .LBB0_572
	s_mov_b64 s[8:9], 0
	v_mov_b32_e32 v0, v213
	v_mov_b32_e32 v2, v212

; __device__ __forceinline__ void phase_ret_scan(const bf16* PROJ, bf16* O, LAS unsigned char* lds, int tid, int vcu, int G) {
;     ...
;         }
;         RS_STORE_O(SEQ / 64 - 1);
.LBB0_651:
	s_and_b64 vcc, exec, s[0:1]
	s_cbranch_vccz .LBB0_568
	v_readlane_b32 s80, v250, 4
	v_readlane_b32 s81, v250, 5
	v_readlane_b32 s82, v250, 6
	v_readlane_b32 s83, v250, 7
	v_lshrrev_b32_e32 v0, 16, v232
	s_nop 3
	buffer_store_short v232, v224, s[80:83], s22 offen
	buffer_store_short v0, v224, s[80:83], s23 offen
	buffer_store_short v231, v224, s[80:83], s24 offen
	v_lshrrev_b32_e32 v0, 16, v231
	buffer_store_short v0, v224, s[80:83], s25 offen
	buffer_store_short v230, v224, s[80:83], s28 offen
	v_lshrrev_b32_e32 v0, 16, v230
	buffer_store_short v0, v224, s[80:83], s29 offen
	buffer_store_short v229, v224, s[80:83], s30 offen
	v_lshrrev_b32_e32 v0, 16, v229
	buffer_store_short v0, v224, s[80:83], s31 offen
	buffer_store_short v228, v224, s[80:83], s33 offen
	v_lshrrev_b32_e32 v0, 16, v228
	buffer_store_short v0, v224, s[80:83], s34 offen
	buffer_store_short v227, v224, s[80:83], s35 offen
	v_lshrrev_b32_e32 v0, 16, v227
	buffer_store_short v0, v224, s[80:83], s36 offen
	buffer_store_short v226, v224, s[80:83], s37 offen
	v_lshrrev_b32_e32 v0, 16, v226
	buffer_store_short v0, v224, s[80:83], s38 offen
	buffer_store_short v225, v224, s[80:83], s39 offen
	v_lshrrev_b32_e32 v0, 16, v225
	buffer_store_short v0, v224, s[80:83], s76 offen
	s_branch .LBB0_568
.Lrf_569:
	s_and_saveexec_b64 s[4:5], s[40:41]
	s_cbranch_execz .Lrf_572
	s_mov_b64 s[8:9], 0
	v_mov_b32_e32 v0, v213
	v_mov_b32_e32 v2, v212

; #define LAS __attribute__((address_space(3)))
; __device__ __forceinline__ void phase_ret_scan(const bf16* PROJ, bf16* O, LAS unsigned char* lds, int tid, int vcu, int G) {
;     ...
;         const int b = unit >> 6, h = (unit >> 3) & 7, vsl = unit & 7;
;         const float lg = __log2f(1.0f - exp2f(-5.0f - (float)h));
;         const float g64 = exp2f(64.0f * lg);
;         f32x16 S[2][2];
; #pragma unroll
;         for (int a = 0; a < 2; ++a)
; #pragma unroll
;             for (int c = 0; c < 2; ++c) S[a][c] = zero16();
;         for (int i = tid; i < 33792 / 16; i += 512) *(LAS v4u*)(lds + ST + i * 16) = (v4u){0u, 0u, 0u, 0u};
;         v4u pq[4], pk[4], pv;
;         const __amdgpu_buffer_rsrc_t rsP = __builtin_amdgcn_make_buffer_rsrc((void*)(PROJ + (size_t)b * SEQ * RT_IN), (short)0, SEQ * RT_IN * 2, 0x00020000);
;         const __amdgpu_buffer_rsrc_t rsO = __builtin_amdgcn_make_buffer_rsrc((void*)(O + (size_t)b * SEQ * RT_V), (short)0, SEQ * RT_V * 2, 0x00020000);
;         const int vrow = tid >> 3, vch = tid & 7;
;         const unsigned voq = (unsigned)((tid >> 5) * RT_IN + (tid & 31) * 8) * 2u, vov = (unsigned)(vrow * RT_IN + vch * 8) * 2u;
;         const unsigned soq = (unsigned)(h * 256) * 2u, sok = (unsigned)(2048 + h * 256) * 2u, sov = (unsigned)(4096 + h * 512 + vsl * 64) * 2u;
;     ...
;         RS_PREFETCH(0);
;         float dec[16];
;         { const int a31 = lane & 31, a5 = lane >> 5, w4 = wave & 3, t_i = w4 >> 1, x_i = w4 & 1;
; #pragma unroll
;           for (int r = 0; r < 16; ++r) {
;               if (wave < 4) { const int t = 32 * x_i + a31, s = 32 * t_i + 8 * (r >> 2) + 4 * a5 + (r & 3); dec[r] = (s <= t) ? __builtin_amdgcn_exp2f((float)(t - s) * lg) : 0.f; }
;               else { const int t = 32 * t_i + (r & 3) + 8 * (r >> 2) + 4 * a5; dec[r] = __builtin_amdgcn_exp2f((float)(t + 1) * lg); } } }
;         unsigned opk[8];
; #pragma unroll
;         for (int i = 0; i < 8; ++i) opk[i] = 0u;
.Lrf_636:
	s_ashr_i32 s27, s26, 31
	s_lshr_b32 s80, s79, 3
	s_lshl_b64 s[4:5], s[26:27], 25
	v_readlane_b32 s92, v250, 4
	s_add_u32 s92, s7, s4
	s_addc_u32 s81, s11, s5
	s_and_b32 s4, s80, 7
	s_lshl_b32 s5, s4, 10
	s_lshl_b32 s27, s4, 9
	v_mul_f32_e32 v2, 0x42800000, v0
	s_mov_b32 s4, 0xc2fc0000
	s_lshl_b32 s26, s78, 1
	v_cmp_gt_f32_e32 vcc, s4, v2
	s_and_b32 s26, s26, 0x380
	s_or_b32 s5, s5, s26
	v_cndmask_b32_e32 v2, 0, v197, vcc
	v_fmac_f32_e32 v2, 0x42800000, v0
	s_or_b32 s26, s5, 0x182000
	v_exp_f32_e32 v2, v2
	v_mul_f32_e32 v0, v0, v169
	v_readlane_b32 s93, v250, 5
	s_and_b64 s[4:5], vcc, exec
	v_exp_f32_e32 v150, v0
	v_readlane_b32 s94, v250, 6
	v_readlane_b32 s95, v250, 7
	s_cselect_b32 s4, 0xffffffc0, 0
	s_and_b32 s93, s81, 0xffff
	v_or_b32_e32 v0, s9, v170
	v_writelane_b32 v250, s92, 4
	v_or_b32_e32 v0, s8, v0
	v_mov_b32_e32 v14, v1
	v_mov_b32_e32 v15, v1
	v_ldexp_f32 v148, v2, s4
	v_writelane_b32 v250, s93, 5
	v_lshlrev_b32_e32 v224, 1, v0
	v_mov_b32_e32 v0, v1
	v_mov_b32_e32 v2, v1
	v_mov_b32_e32 v3, v1
	v_mov_b32_e32 v4, v1
	v_mov_b32_e32 v5, v1
	v_mov_b32_e32 v6, v1
	v_mov_b32_e32 v7, v1
	v_mov_b32_e32 v8, v1
	v_mov_b32_e32 v9, v1
	v_mov_b32_e32 v10, v1
	v_mov_b32_e32 v11, v1
	v_mov_b32_e32 v12, v1
	v_mov_b32_e32 v13, v1
	s_waitcnt vmcnt(13)
	v_mov_b64_e32 v[30:31], v[14:15]
	v_mov_b64_e32 v[46:47], v[14:15]
	v_mov_b64_e32 v[62:63], v[14:15]
	v_mov_b64_e32 v[78:79], v[14:15]
	s_mov_b32 s80, 0
	v_writelane_b32 v250, s94, 6
	v_mov_b32_e32 v151, v150
	v_mov_b32_e32 v152, v148
	v_mov_b32_e32 v153, v148
	v_mov_b32_e32 v225, 0
	v_mov_b32_e32 v226, 0
	v_mov_b32_e32 v227, 0
	v_mov_b32_e32 v228, 0
	v_mov_b32_e32 v229, 0
	v_mov_b32_e32 v230, 0
	v_mov_b32_e32 v231, 0
	v_mov_b32_e32 v232, 0
	s_mov_b32 s81, 0
	v_mov_b64_e32 v[28:29], v[12:13]
	v_mov_b64_e32 v[26:27], v[10:11]
	v_mov_b64_e32 v[24:25], v[8:9]
	v_mov_b64_e32 v[22:23], v[6:7]
	v_mov_b64_e32 v[20:21], v[4:5]
	v_mov_b64_e32 v[18:19], v[2:3]
	v_mov_b64_e32 v[16:17], v[0:1]
	v_mov_b64_e32 v[44:45], v[12:13]
	v_mov_b64_e32 v[42:43], v[10:11]
	v_mov_b64_e32 v[40:41], v[8:9]
	v_mov_b64_e32 v[38:39], v[6:7]
	v_mov_b64_e32 v[36:37], v[4:5]
	v_mov_b64_e32 v[34:35], v[2:3]
	v_mov_b64_e32 v[32:33], v[0:1]
	v_mov_b64_e32 v[60:61], v[12:13]
	v_mov_b64_e32 v[58:59], v[10:11]
	v_mov_b64_e32 v[56:57], v[8:9]
	v_mov_b64_e32 v[54:55], v[6:7]
	v_mov_b64_e32 v[52:53], v[4:5]
	v_mov_b64_e32 v[50:51], v[2:3]
	v_mov_b64_e32 v[48:49], v[0:1]
	v_mov_b64_e32 v[76:77], v[12:13]
	v_mov_b64_e32 v[74:75], v[10:11]
	v_mov_b64_e32 v[72:73], v[8:9]
	v_mov_b64_e32 v[70:71], v[6:7]
	v_mov_b64_e32 v[68:69], v[4:5]
	v_mov_b64_e32 v[66:67], v[2:3]
	v_mov_b64_e32 v[64:65], v[0:1]
	v_writelane_b32 v250, s95, 7
	s_nop 1
	v_readlane_b32 s92, v250, 0
	v_readlane_b32 s93, v250, 1
	v_readlane_b32 s94, v250, 2
	v_readlane_b32 s95, v250, 3
	s_add_i32 s4, s27, 0x180000
	s_add_i32 s5, s27, 0x181000
	s_nop 4
	buffer_load_dwordx4 v[170:173], v167, s[92:95], s4 offen
	buffer_load_dwordx4 v[174:177], v167, s[92:95], s5 offen
	s_add_i32 s4, s27, 0x1e0000
	s_add_i32 s5, s27, 0x1e1000
	buffer_load_dwordx4 v[178:181], v167, s[92:95], s4 offen
	buffer_load_dwordx4 v[182:185], v167, s[92:95], s5 offen
	s_add_i32 s4, s27, 0x240000
	s_add_i32 s5, s27, 0x241000
	buffer_load_dwordx4 v[186:189], v167, s[92:95], s4 offen
	buffer_load_dwordx4 v[202:205], v167, s[92:95], s5 offen
	s_add_i32 s4, s27, 0x2a0000
	s_add_i32 s5, s27, 0x2a1000
	buffer_load_dwordx4 v[206:209], v167, s[92:95], s4 offen
	buffer_load_dwordx4 v[238:241], v167, s[92:95], s5 offen
	buffer_load_dwordx4 v[244:247], v168, s[92:95], s26 offen
	s_branch .Lrf_639

; #define LAS __attribute__((address_space(3)))
; __device__ __forceinline__ v4u scale_bf8(v4u q, float f) { v4u o; o.x = pk2(bflo(q.x) * f, bfhi(q.x) * f); o.y = pk2(bflo(q.y) * f, bfhi(q.y) * f); o.z = pk2(bflo(q.z) * f, bfhi(q.z) * f); o.w = pk2(bflo(q.w) * f, bfhi(q.w) * f); return o; }
; __device__ __forceinline__ void phase_ret_scan(const bf16* PROJ, bf16* O, LAS unsigned char* lds, int tid, int vcu, int G) {
;     ...
;         for (int ch = 0; ch < SEQ / 64; ++ch) {
; #pragma unroll
;             for (int i = 0; i < 4; ++i) { const int cid = tid + 512 * i, row = cid >> 5, chq = cid & 31;
;                 *(LAS v4u*)(lds + QN + row * QRS + chq * 16) = pq[i];
;                 *(LAS v4u*)(lds + KN + (chq >> 4) * 16384 + off_b(row, chq & 15)) = pk[i]; }
;             *(LAS v4u*)(lds + VV + off_b(vrow, vch)) = pv;
;             *(LAS v4u*)(lds + VV + off_b(vrow, 8 + vch)) = scale_bf8(pv, __builtin_amdgcn_exp2f((float)(63 - vrow) * lg));
;             __syncthreads();
;     ...
;             if (ch > 0) RS_STORE_O(ch - 1);
;             if (ch + 1 < SEQ / 64) RS_PREFETCH(ch + 1);
.Lrf_639:
	s_bitcmp1_b32 s81, 19
	s_cbranch_scc1 .Lrf_topB
	s_waitcnt vmcnt(9)
	v_lshlrev_b32_e32 v2, 16, v128
	v_and_b32_e32 v3, 0xffff0000, v128
	v_lshlrev_b32_e32 v4, 16, v129
	v_and_b32_e32 v5, 0xffff0000, v129
	v_pk_mul_f32 v[2:3], v[150:151], v[2:3]
	v_pk_mul_f32 v[4:5], v[150:151], v[4:5]
	s_cmp_lg_u32 s81, 0
	v_cvt_pk_bf16_f32 v2, v2, v3
	v_cvt_pk_bf16_f32 v3, v4, v5
	v_lshlrev_b32_e32 v4, 16, v130
	v_and_b32_e32 v5, 0xffff0000, v130
	v_lshlrev_b32_e32 v6, 16, v131
	v_and_b32_e32 v7, 0xffff0000, v131
	s_cselect_b64 s[4:5], -1, 0
	v_pk_mul_f32 v[4:5], v[150:151], v[4:5]
	v_pk_mul_f32 v[6:7], v[150:151], v[6:7]
	s_and_b64 s[4:5], s[4:5], s[0:1]
	v_cvt_pk_bf16_f32 v4, v4, v5
	v_cvt_pk_bf16_f32 v5, v6, v7
	s_and_b64 vcc, exec, s[4:5]
	ds_write_b128 v214, v[96:99]
	ds_write_b128 v215, v[100:103] offset:33792
	ds_write_b128 v216, v[104:107]
	ds_write_b128 v217, v[108:111] offset:33792
	ds_write_b128 v218, v[112:115]
	ds_write_b128 v219, v[116:119] offset:33792
	ds_write_b128 v220, v[120:123]
	ds_write_b128 v221, v[124:127] offset:33792
	ds_write_b128 v222, v[128:131]
	ds_write_b128 v223, v[2:5]
	s_waitcnt lgkmcnt(0)
	s_barrier
	s_cbranch_vccz .Lrf_641A
	s_add_i32 s4, s21, s81
	v_readlane_b32 s92, v250, 4
	s_add_i32 s5, s4, 0xfff80000
	v_readlane_b32 s93, v250, 5
	v_readlane_b32 s94, v250, 6
	v_readlane_b32 s95, v250, 7
	v_lshrrev_b32_e32 v0, 16, v232
	s_nop 3
	buffer_store_short v232, v224, s[92:95], s5 offen
	s_add_i32 s5, s4, 0xfff82000
	buffer_store_short v0, v224, s[92:95], s5 offen
	s_add_i32 s5, s4, 0xfff84000
	buffer_store_short v231, v224, s[92:95], s5 offen
	v_lshrrev_b32_e32 v0, 16, v231
	s_add_i32 s5, s4, 0xfff86000
	buffer_store_short v0, v224, s[92:95], s5 offen
	s_add_i32 s5, s4, 0xfff90000
	buffer_store_short v230, v224, s[92:95], s5 offen
	v_lshrrev_b32_e32 v0, 16, v230
	s_add_i32 s5, s4, 0xfff92000
	buffer_store_short v0, v224, s[92:95], s5 offen
	s_add_i32 s5, s4, 0xfff94000
	buffer_store_short v229, v224, s[92:95], s5 offen
	v_lshrrev_b32_e32 v0, 16, v229
	s_add_i32 s5, s4, 0xfff96000
	buffer_store_short v0, v224, s[92:95], s5 offen
	s_add_i32 s5, s4, 0xfffa0000
	buffer_store_short v228, v224, s[92:95], s5 offen
	v_lshrrev_b32_e32 v0, 16, v228
	s_add_i32 s5, s4, 0xfffa2000
	buffer_store_short v0, v224, s[92:95], s5 offen
	s_add_i32 s5, s4, 0xfffa4000
	buffer_store_short v227, v224, s[92:95], s5 offen
	v_lshrrev_b32_e32 v0, 16, v227
	s_add_i32 s5, s4, 0xfffa6000
	buffer_store_short v0, v224, s[92:95], s5 offen
	s_add_i32 s5, s4, 0xfffb0000
	buffer_store_short v226, v224, s[92:95], s5 offen
	v_lshrrev_b32_e32 v0, 16, v226
	s_add_i32 s5, s4, 0xfffb2000
	buffer_store_short v0, v224, s[92:95], s5 offen
	s_add_i32 s5, s4, 0xfffb4000
	v_lshrrev_b32_e32 v0, 16, v225
	s_add_i32 s4, s4, 0xfffb6000
	buffer_store_short v225, v224, s[92:95], s5 offen
	buffer_store_short v0, v224, s[92:95], s4 offen
.Lrf_641A:
	s_cmp_ge_u32 s81, 0x1f00000
	s_cbranch_scc1 .Lrf_643
	s_add_i32 s4, s27, s80
	v_readlane_b32 s92, v250, 0
	s_add_i32 s5, s4, 0x300000
	v_readlane_b32 s93, v250, 1
	v_readlane_b32 s94, v250, 2
	v_readlane_b32 s95, v250, 3
	s_nop 4
	buffer_load_dwordx4 v[96:99], v167, s[92:95], s5 offen
	s_add_i32 s5, s4, 0x301000
	buffer_load_dwordx4 v[100:103], v167, s[92:95], s5 offen
	s_add_i32 s5, s4, 0x360000
	buffer_load_dwordx4 v[104:107], v167, s[92:95], s5 offen
	s_add_i32 s5, s4, 0x361000
	buffer_load_dwordx4 v[108:111], v167, s[92:95], s5 offen
	s_add_i32 s5, s4, 0x3c0000
	buffer_load_dwordx4 v[112:115], v167, s[92:95], s5 offen
	s_add_i32 s5, s4, 0x3c1000
	buffer_load_dwordx4 v[116:119], v167, s[92:95], s5 offen
	s_add_i32 s5, s4, 0x420000
	s_add_i32 s4, s4, 0x421000
	buffer_load_dwordx4 v[120:123], v167, s[92:95], s5 offen
	buffer_load_dwordx4 v[124:127], v167, s[92:95], s4 offen
	s_add_i32 s4, s26, s80
	s_add_i32 s4, s4, 0x180000
	buffer_load_dwordx4 v[128:131], v168, s[92:95], s4 offen
	s_branch .Lrf_643
.Lrf_topB:
	s_cmp_eq_u32 s81, 0x1f80000
	s_cbranch_scc1 .Lrf_topB_last
	s_waitcnt vmcnt(9)
	s_branch .Lrf_topB_go

; #define LAS __attribute__((address_space(3)))
; __device__ __forceinline__ v4u scale_bf8(v4u q, float f) { v4u o; o.x = pk2(bflo(q.x) * f, bfhi(q.x) * f); o.y = pk2(bflo(q.y) * f, bfhi(q.y) * f); o.z = pk2(bflo(q.z) * f, bfhi(q.z) * f); o.w = pk2(bflo(q.w) * f, bfhi(q.w) * f); return o; }
; __device__ __forceinline__ void phase_ret_scan(const bf16* PROJ, bf16* O, LAS unsigned char* lds, int tid, int vcu, int G) {
;     ...
;         for (int ch = 0; ch < SEQ / 64; ++ch) {
; #pragma unroll
;             for (int i = 0; i < 4; ++i) { const int cid = tid + 512 * i, row = cid >> 5, chq = cid & 31;
;                 *(LAS v4u*)(lds + QN + row * QRS + chq * 16) = pq[i];
;                 *(LAS v4u*)(lds + KN + (chq >> 4) * 16384 + off_b(row, chq & 15)) = pk[i]; }
;             *(LAS v4u*)(lds + VV + off_b(vrow, vch)) = pv;
;             *(LAS v4u*)(lds + VV + off_b(vrow, 8 + vch)) = scale_bf8(pv, __builtin_amdgcn_exp2f((float)(63 - vrow) * lg));
;             __syncthreads();
;     ...
;             if (ch > 0) RS_STORE_O(ch - 1);
;             if (ch + 1 < SEQ / 64) RS_PREFETCH(ch + 1);
.Lrf_topB_go:
	v_lshlrev_b32_e32 v2, 16, v244
	v_and_b32_e32 v3, 0xffff0000, v244
	v_lshlrev_b32_e32 v4, 16, v245
	v_and_b32_e32 v5, 0xffff0000, v245
	v_pk_mul_f32 v[2:3], v[150:151], v[2:3]
	v_pk_mul_f32 v[4:5], v[150:151], v[4:5]
	s_cmp_lg_u32 s81, 0
	v_cvt_pk_bf16_f32 v2, v2, v3
	v_cvt_pk_bf16_f32 v3, v4, v5
	v_lshlrev_b32_e32 v4, 16, v246
	v_and_b32_e32 v5, 0xffff0000, v246
	v_lshlrev_b32_e32 v6, 16, v247
	v_and_b32_e32 v7, 0xffff0000, v247
	s_cselect_b64 s[4:5], -1, 0
	v_pk_mul_f32 v[4:5], v[150:151], v[4:5]
	v_pk_mul_f32 v[6:7], v[150:151], v[6:7]
	s_and_b64 s[4:5], s[4:5], s[0:1]
	v_cvt_pk_bf16_f32 v4, v4, v5
	v_cvt_pk_bf16_f32 v5, v6, v7
	s_and_b64 vcc, exec, s[4:5]
	ds_write_b128 v214, v[170:173]
	ds_write_b128 v215, v[174:177] offset:33792
	ds_write_b128 v216, v[178:181]
	ds_write_b128 v217, v[182:185] offset:33792
	ds_write_b128 v218, v[186:189]
	ds_write_b128 v219, v[202:205] offset:33792
	ds_write_b128 v220, v[206:209]
	ds_write_b128 v221, v[238:241] offset:33792
	ds_write_b128 v222, v[244:247]
	ds_write_b128 v223, v[2:5]
	s_waitcnt lgkmcnt(0)
	s_barrier
	s_cbranch_vccz .Lrf_641B
	s_add_i32 s4, s21, s81
	v_readlane_b32 s92, v250, 4
	s_add_i32 s5, s4, 0xfff80000
	v_readlane_b32 s93, v250, 5
	v_readlane_b32 s94, v250, 6
	v_readlane_b32 s95, v250, 7
	v_lshrrev_b32_e32 v0, 16, v232
	s_nop 3
	buffer_store_short v232, v224, s[92:95], s5 offen
	s_add_i32 s5, s4, 0xfff82000
	buffer_store_short v0, v224, s[92:95], s5 offen
	s_add_i32 s5, s4, 0xfff84000
	buffer_store_short v231, v224, s[92:95], s5 offen
	v_lshrrev_b32_e32 v0, 16, v231
	s_add_i32 s5, s4, 0xfff86000
	buffer_store_short v0, v224, s[92:95], s5 offen
	s_add_i32 s5, s4, 0xfff90000
	buffer_store_short v230, v224, s[92:95], s5 offen
	v_lshrrev_b32_e32 v0, 16, v230
	s_add_i32 s5, s4, 0xfff92000
	buffer_store_short v0, v224, s[92:95], s5 offen
	s_add_i32 s5, s4, 0xfff94000
	buffer_store_short v229, v224, s[92:95], s5 offen
	v_lshrrev_b32_e32 v0, 16, v229
	s_add_i32 s5, s4, 0xfff96000
	buffer_store_short v0, v224, s[92:95], s5 offen
	s_add_i32 s5, s4, 0xfffa0000
	buffer_store_short v228, v224, s[92:95], s5 offen
	v_lshrrev_b32_e32 v0, 16, v228
	s_add_i32 s5, s4, 0xfffa2000
	buffer_store_short v0, v224, s[92:95], s5 offen
	s_add_i32 s5, s4, 0xfffa4000
	buffer_store_short v227, v224, s[92:95], s5 offen
	v_lshrrev_b32_e32 v0, 16, v227
	s_add_i32 s5, s4, 0xfffa6000
	buffer_store_short v0, v224, s[92:95], s5 offen
	s_add_i32 s5, s4, 0xfffb0000
	buffer_store_short v226, v224, s[92:95], s5 offen
	v_lshrrev_b32_e32 v0, 16, v226
	s_add_i32 s5, s4, 0xfffb2000
	buffer_store_short v0, v224, s[92:95], s5 offen
	s_add_i32 s5, s4, 0xfffb4000
	v_lshrrev_b32_e32 v0, 16, v225
	s_add_i32 s4, s4, 0xfffb6000
	buffer_store_short v225, v224, s[92:95], s5 offen
	buffer_store_short v0, v224, s[92:95], s4 offen
.Lrf_641B:
	s_cmp_ge_u32 s81, 0x1f00000
	s_cbranch_scc1 .Lrf_643
	s_add_i32 s4, s27, s80
	v_readlane_b32 s92, v250, 0
	s_add_i32 s5, s4, 0x300000
	v_readlane_b32 s93, v250, 1
	v_readlane_b32 s94, v250, 2
	v_readlane_b32 s95, v250, 3
	s_nop 4
	buffer_load_dwordx4 v[170:173], v167, s[92:95], s5 offen
	s_add_i32 s5, s4, 0x301000
	buffer_load_dwordx4 v[174:177], v167, s[92:95], s5 offen
	s_add_i32 s5, s4, 0x360000
	buffer_load_dwordx4 v[178:181], v167, s[92:95], s5 offen
	s_add_i32 s5, s4, 0x361000
	buffer_load_dwordx4 v[182:185], v167, s[92:95], s5 offen
	s_add_i32 s5, s4, 0x3c0000
	buffer_load_dwordx4 v[186:189], v167, s[92:95], s5 offen
	s_add_i32 s5, s4, 0x3c1000
	buffer_load_dwordx4 v[202:205], v167, s[92:95], s5 offen
	s_add_i32 s5, s4, 0x420000
	s_add_i32 s4, s4, 0x421000
	buffer_load_dwordx4 v[206:209], v167, s[92:95], s5 offen
	buffer_load_dwordx4 v[238:241], v167, s[92:95], s4 offen
	s_add_i32 s4, s26, s80
	s_add_i32 s4, s4, 0x180000
	buffer_load_dwordx4 v[244:247], v168, s[92:95], s4 offen

; #define LAS __attribute__((address_space(3)))
; __device__ __forceinline__ unsigned pk2(float lo, float hi) { const pk_f2 v = {lo, hi}; return __builtin_bit_cast(unsigned, __builtin_convertvector(v, pk_b2)); }
; #define RS_LD1A(fa, fb, g4) do { _Pragma("unroll") for (int j = 0; j < 2; ++j) { const int ks = 2 * (g4) + j; \
;                     fa[j] = *(const LAS s16x8*)(lds + KN + (ks >> 3) * 16384 + off_b(32 * si + a31, 2 * (ks & 7) + a5)); \
;                     fb[j] = *(const LAS s16x8*)(lds + QN + (32 * ti + a31) * QRS + (16 * ks + 8 * a5) * 2); } } while (0)
; #define RS_MMA2(fa, fb) do { _Pragma("unroll") for (int j = 0; j < 2; ++j) acc = mfma32(fa[j], fb[j], acc); } while (0)
; __device__ __forceinline__ void phase_ret_scan(const bf16* PROJ, bf16* O, LAS unsigned char* lds, int tid, int vcu, int G) {
;     ...
;             if (wave < 4) {
;                 const int si = t_i, ti = x_i;
;     ...
;                 RS_LD1A(fa0, fb0, 0); RS_LD1A(fa1, fb1, 1);
; #pragma unroll
;                 for (int g2 = 0; g2 < 3; ++g2) { RS_MMA2(fa0, fb0); RS_LD1A(fa0, fb0, 2 * g2 + 2); RS_MMA2(fa1, fb1); RS_LD1A(fa1, fb1, 2 * g2 + 3); }
;                 RS_MMA2(fa0, fb0); RS_MMA2(fa1, fb1);
;     ...
;                 const int t = 32 * ti + a31;
; #pragma unroll
;                 for (int g = 0; g < 4; ++g) { float pvv[4];
; #pragma unroll
;                     for (int e = 0; e < 4; ++e) pvv[e] = acc[4 * g + e] * dec[4 * g + e];
;                     v2u w; w.x = pk2(pvv[0], pvv[1]); w.y = pk2(pvv[2], pvv[3]);
;                     *(LAS v2u*)(lds + PI + t * PRS + (32 * si + 8 * g + 4 * a5) * 2) = w; }
.Lrf_645:
	s_andn2_b64 vcc, exec, s[4:5]
	s_cbranch_vccnz .Lrf_647
	v_lshlrev_b32_e32 v4, 2, v0
	v_and_b32_e32 v12, 12, v4
	v_bfe_u32 v13, v2, 2, 2
	v_lshl_add_u32 v14, v0, 8, s14
	v_bitop3_b32 v4, v12, v3, v13 bitop3:0x36
	v_readlane_b32 s4, v250, 13
	v_lshl_add_u32 v243, v4, 4, v14
	v_or_b32_e32 v15, s13, v0
	v_mul_u32_u24_e32 v8, 0x210, v15
	v_lshlrev_b32_e32 v9, 4, v3
	v_add3_u32 v242, 0, v8, v9
	v_lshlrev_b32_e32 v255, 3, v3
	v_mov_b32_e32 v248, s4
	s_movk_i32 s4, 0x90
	v_mad_u32_u24 v248, v15, s4, v248
	v_add3_u32 v149, v248, v255, s15
	ds_read_b128 v[4:7], v243 offset:33792
	ds_read_b128 v[8:11], v242
	v_xor_b32_e32 v254, 32, v243
	ds_read_b128 v[12:15], v254 offset:33792
	ds_read_b128 v[226:229], v242 offset:32
	v_xor_b32_e32 v253, 64, v243
	ds_read_b128 v[230:233], v253 offset:33792
	ds_read_b128 v[210:213], v242 offset:64
	s_waitcnt lgkmcnt(4)
	v_mfma_f32_32x32x16_bf16 v[80:95], v[4:7], v[8:11], 0
	v_xor_b32_e32 v254, 0x60, v243
	ds_read_b128 v[4:7], v254 offset:33792
	ds_read_b128 v[8:11], v242 offset:96
	s_waitcnt lgkmcnt(4)
	v_mfma_f32_32x32x16_bf16 v[80:95], v[12:15], v[226:229], v[80:95]
	v_xor_b32_e32 v253, 0x80, v243
	ds_read_b128 v[12:15], v253 offset:33792
	ds_read_b128 v[226:229], v242 offset:128
	s_waitcnt lgkmcnt(4)
	v_mfma_f32_32x32x16_bf16 v[80:95], v[230:233], v[210:213], v[80:95]
	v_xor_b32_e32 v254, 0xa0, v243
	ds_read_b128 v[230:233], v254 offset:33792
	ds_read_b128 v[210:213], v242 offset:160
	s_waitcnt lgkmcnt(4)
	v_mfma_f32_32x32x16_bf16 v[80:95], v[4:7], v[8:11], v[80:95]
	v_xor_b32_e32 v253, 0xc0, v243
	ds_read_b128 v[4:7], v253 offset:33792
	ds_read_b128 v[8:11], v242 offset:192
	s_waitcnt lgkmcnt(4)
	v_mfma_f32_32x32x16_bf16 v[80:95], v[12:15], v[226:229], v[80:95]
	v_xor_b32_e32 v254, 0xe0, v243
	ds_read_b128 v[12:15], v254 offset:33792
	ds_read_b128 v[226:229], v242 offset:224
	s_waitcnt lgkmcnt(4)
	v_mfma_f32_32x32x16_bf16 v[80:95], v[230:233], v[210:213], v[80:95]
	ds_read_b128 v[230:233], v243 offset:50176
	ds_read_b128 v[210:213], v242 offset:256
	s_waitcnt lgkmcnt(4)
	v_mfma_f32_32x32x16_bf16 v[80:95], v[4:7], v[8:11], v[80:95]
	v_xor_b32_e32 v254, 32, v243
	ds_read_b128 v[4:7], v254 offset:50176
	ds_read_b128 v[8:11], v242 offset:288
	s_waitcnt lgkmcnt(4)
	v_mfma_f32_32x32x16_bf16 v[80:95], v[12:15], v[226:229], v[80:95]
	v_xor_b32_e32 v253, 64, v243
	ds_read_b128 v[12:15], v253 offset:50176
	ds_read_b128 v[226:229], v242 offset:320
	s_waitcnt lgkmcnt(4)
	v_mfma_f32_32x32x16_bf16 v[80:95], v[230:233], v[210:213], v[80:95]
	v_xor_b32_e32 v254, 0x60, v243
	ds_read_b128 v[230:233], v254 offset:50176
	ds_read_b128 v[210:213], v242 offset:352
	s_waitcnt lgkmcnt(4)
	v_mfma_f32_32x32x16_bf16 v[80:95], v[4:7], v[8:11], v[80:95]
	v_xor_b32_e32 v253, 0x80, v243
	ds_read_b128 v[4:7], v253 offset:50176
	ds_read_b128 v[8:11], v242 offset:384
	s_waitcnt lgkmcnt(4)
	v_mfma_f32_32x32x16_bf16 v[80:95], v[12:15], v[226:229], v[80:95]
	v_xor_b32_e32 v254, 0xa0, v243
	ds_read_b128 v[12:15], v254 offset:50176
	ds_read_b128 v[226:229], v242 offset:416
	s_waitcnt lgkmcnt(4)
	v_mfma_f32_32x32x16_bf16 v[80:95], v[230:233], v[210:213], v[80:95]
	v_xor_b32_e32 v253, 0xc0, v243
	ds_read_b128 v[230:233], v253 offset:50176
	ds_read_b128 v[210:213], v242 offset:448
	s_waitcnt lgkmcnt(4)
	v_mfma_f32_32x32x16_bf16 v[80:95], v[4:7], v[8:11], v[80:95]
	v_xor_b32_e32 v254, 0xe0, v243
	ds_read_b128 v[4:7], v254 offset:50176
	ds_read_b128 v[8:11], v242 offset:480
	s_waitcnt lgkmcnt(4)
	v_mfma_f32_32x32x16_bf16 v[80:95], v[12:15], v[226:229], v[80:95]
	s_waitcnt lgkmcnt(2)
	v_mfma_f32_32x32x16_bf16 v[80:95], v[230:233], v[210:213], v[80:95]
	s_waitcnt lgkmcnt(0)
	v_mfma_f32_32x32x16_bf16 v[80:95], v[4:7], v[8:11], v[80:95]
	s_nop 11
	v_pk_mul_f32 v[4:5], v[132:133], v[80:81]
	v_pk_mul_f32 v[6:7], v[134:135], v[82:83]
	v_pk_mul_f32 v[8:9], v[136:137], v[84:85]
	v_pk_mul_f32 v[10:11], v[138:139], v[86:87]
	v_pk_mul_f32 v[12:13], v[140:141], v[88:89]
	v_pk_mul_f32 v[14:15], v[142:143], v[90:91]
	v_pk_mul_f32 v[210:211], v[144:145], v[92:93]
	v_pk_mul_f32 v[212:213], v[146:147], v[94:95]
	v_cvt_pk_bf16_f32 v4, v4, v5
	v_cvt_pk_bf16_f32 v5, v6, v7
	v_cvt_pk_bf16_f32 v6, v8, v9
	v_cvt_pk_bf16_f32 v7, v10, v11
	v_cvt_pk_bf16_f32 v8, v12, v13
	v_cvt_pk_bf16_f32 v9, v14, v15
	v_cvt_pk_bf16_f32 v10, v210, v211
	v_cvt_pk_bf16_f32 v11, v212, v213
	ds_write2_b64 v149, v[4:5], v[6:7] offset1:2
	ds_write2_b64 v149, v[8:9], v[10:11] offset0:4 offset1:6

; __global__ void __launch_bounds__(NWAVES * 64, 2) trunk_fwd(Args a) {
;     extern __shared__ __attribute__((aligned(16))) unsigned char lds_raw[];
	.amdhsa_kernel _Z9trunk_fwd4Args
		.amdhsa_group_segment_fixed_size 0
		.amdhsa_private_segment_fixed_size 0
		.amdhsa_kernarg_size 432
		.amdhsa_user_sgpr_count 2
		.amdhsa_user_sgpr_dispatch_ptr 0
		.amdhsa_user_sgpr_queue_ptr 0
		.amdhsa_user_sgpr_kernarg_segment_ptr 1
		.amdhsa_user_sgpr_dispatch_id 0
		.amdhsa_user_sgpr_kernarg_preload_length 0
		.amdhsa_user_sgpr_kernarg_preload_offset 0
		.amdhsa_user_sgpr_private_segment_size 0
		.amdhsa_uses_dynamic_stack 0
		.amdhsa_enable_private_segment 0
		.amdhsa_system_sgpr_workgroup_id_x 1
		.amdhsa_system_sgpr_workgroup_id_y 0
		.amdhsa_system_sgpr_workgroup_id_z 0
		.amdhsa_system_sgpr_workgroup_info 0
		.amdhsa_system_vgpr_workitem_id 0
		.amdhsa_next_free_vgpr 256
		.amdhsa_next_free_sgpr 98
		.amdhsa_accum_offset 256
		.amdhsa_reserve_vcc 1
		.amdhsa_float_round_mode_32 0
		.amdhsa_float_round_mode_16_64 0
		.amdhsa_float_denorm_mode_32 3
		.amdhsa_float_denorm_mode_16_64 3
		.amdhsa_dx10_clamp 1
		.amdhsa_ieee_mode 1
		.amdhsa_fp16_overflow 0
		.amdhsa_tg_split 0
		.amdhsa_exception_fp_ieee_invalid_op 0
		.amdhsa_exception_fp_denorm_src 0
		.amdhsa_exception_fp_ieee_div_zero 0
		.amdhsa_exception_fp_ieee_overflow 0
		.amdhsa_exception_fp_ieee_underflow 0
		.amdhsa_exception_fp_ieee_inexact 0
		.amdhsa_exception_int_div_zero 0
	.end_amdhsa_kernel

; __global__ void __launch_bounds__(NWAVES * 64, 2) trunk_fwd(Args a) {
;     extern __shared__ __attribute__((aligned(16))) unsigned char lds_raw[];
amdhsa.kernels:
  - .agpr_count:     0
    .args:
      - .offset:         0
        .size:           176
        .value_kind:     by_value
      - .offset:         176
        .size:           4
        .value_kind:     hidden_block_count_x
      - .offset:         180
        .size:           4
        .value_kind:     hidden_block_count_y
      - .offset:         184
        .size:           4
        .value_kind:     hidden_block_count_z
      - .offset:         188
        .size:           2
        .value_kind:     hidden_group_size_x
      - .offset:         190
        .size:           2
        .value_kind:     hidden_group_size_y
      - .offset:         192
        .size:           2
        .value_kind:     hidden_group_size_z
      - .offset:         194
        .size:           2
        .value_kind:     hidden_remainder_x
      - .offset:         196
        .size:           2
        .value_kind:     hidden_remainder_y
      - .offset:         198
        .size:           2
        .value_kind:     hidden_remainder_z
      - .offset:         216
        .size:           8
        .value_kind:     hidden_global_offset_x
      - .offset:         224
        .size:           8
        .value_kind:     hidden_global_offset_y
      - .offset:         232
        .size:           8
        .value_kind:     hidden_global_offset_z
      - .offset:         240
        .size:           2
        .value_kind:     hidden_grid_dims
      - .offset:         296
        .size:           4
        .value_kind:     hidden_dynamic_lds_size
    .group_segment_fixed_size: 0
    .kernarg_segment_align: 8
    .kernarg_segment_size: 432
    .language:       OpenCL C
    .language_version:
      - 2
      - 0
    .max_flat_workgroup_size: 512
    .name:           _Z9trunk_fwd4Args
    .private_segment_fixed_size: 0
    .sgpr_count:     104
    .sgpr_spill_count: 385
    .symbol:         _Z9trunk_fwd4Args.kd
    .uniform_work_group_size: 1
    .uses_dynamic_stack: false
    .vgpr_count:     256
    .vgpr_spill_count: 0
    .wavefront_size: 64
